# loop-edge edit: diff attention loop B, branch chain after the per-tile barrier shortened by one taken branch (test of DMA-needed inlined at the barrier block)
# speedup vs baseline: 1.0021x; 1.0021x over previous
.LBB0_191:
	s_waitcnt vmcnt(4) lgkmcnt(0)
	s_barrier
	s_cmp_gt_u32 s86, 61
	s_cbranch_scc0 .LBB0_193
	s_branch .LBB0_187
